# residual-update epilogues of dense down and layer-1 out-projection: 13 of 15 serialised residual loads issued up front into dead fragment VGPRs (epilogue de-serialisation)
# baseline (speedup 1.0000x reference)
.LBB0_1540:
	s_ashr_i32 s19, s18, 31
	s_lshl_b64 s[18:19], s[18:19], 20
	v_lshl_or_b32 v10, s51, 8, v169
	s_add_u32 s18, s41, s18
	v_ashrrev_i32_e32 v11, 31, v10
	v_lshl_add_u64 v[14:15], v[10:11], 2, s[20:21]
	s_addc_u32 s19, s42, s19
	global_load_dwordx4 v[2:5], v[14:15], off offset:16
	global_load_dwordx4 v[6:9], v[14:15], off
	v_lshl_add_u64 v[18:19], v[10:11], 1, s[18:19]
	v_lshl_add_u64 v[32:33], v[18:19], 0, v[172:173]
	global_load_dwordx4 v[10:13], v[32:33], off
	global_load_dwordx4 v[20:23], v[14:15], off offset:528
	s_nop 0
	global_load_dwordx4 v[14:17], v[14:15], off offset:512
	s_and_b64 vcc, exec, s[6:7]
	s_mov_b64 s[6:7], -1
	v_lshl_add_u64 v[252:253], v[18:19], 0, v[172:173]
	global_load_dwordx4 v[192:195], v[252:253], off offset:256
	v_lshl_add_u64 v[252:253], v[18:19], 0, v[174:175]
	global_load_dwordx4 v[204:207], v[252:253], off
	global_load_dwordx4 v[208:211], v[252:253], off offset:256
	v_lshl_add_u64 v[252:253], v[18:19], 0, v[176:177]
	global_load_dwordx4 v[212:215], v[252:253], off
	global_load_dwordx4 v[216:219], v[252:253], off offset:256
	v_lshl_add_u64 v[252:253], v[18:19], 0, v[178:179]
	global_load_dwordx4 v[220:223], v[252:253], off
	global_load_dwordx4 v[224:227], v[252:253], off offset:256
	v_lshl_add_u64 v[252:253], v[18:19], 0, v[180:181]
	global_load_dwordx4 v[228:231], v[252:253], off
	global_load_dwordx4 v[232:235], v[252:253], off offset:256
	v_lshl_add_u64 v[252:253], v[18:19], 0, v[182:183]
	global_load_dwordx4 v[236:239], v[252:253], off
	global_load_dwordx4 v[240:243], v[252:253], off offset:256
	v_lshl_add_u64 v[252:253], v[18:19], 0, v[184:185]
	global_load_dwordx4 v[244:247], v[252:253], off
	global_load_dwordx4 v[248:251], v[252:253], off offset:256
	s_waitcnt vmcnt(13)
	v_pk_mul_f32 v[2:3], v[2:3], s[14:15] op_sel_hi:[1,0]
	v_pk_mul_f32 v[6:7], v[6:7], s[14:15] op_sel_hi:[1,0]
	v_lshlrev_b32_e32 v24, 16, v10
	v_and_b32_e32 v25, 0xffff0000, v10
	v_lshlrev_b32_e32 v26, 16, v12
	v_and_b32_e32 v27, 0xffff0000, v12
	v_pk_mul_f32 v[8:9], v[8:9], s[14:15] op_sel_hi:[1,0]
	v_pk_mul_f32 v[4:5], v[4:5], s[14:15] op_sel_hi:[1,0]
	v_lshlrev_b32_e32 v10, 16, v11
	v_and_b32_e32 v11, 0xffff0000, v11
	v_lshlrev_b32_e32 v12, 16, v13
	v_and_b32_e32 v13, 0xffff0000, v13
	v_pk_fma_f32 v[24:25], v[158:159], v[6:7], v[24:25]
	v_pk_fma_f32 v[26:27], v[154:155], v[2:3], v[26:27]
	v_pk_fma_f32 v[10:11], v[160:161], v[8:9], v[10:11]
	v_pk_fma_f32 v[12:13], v[156:157], v[4:5], v[12:13]
	v_cvt_pk_bf16_f32 v24, v24, v25
	v_cvt_pk_bf16_f32 v25, v10, v11
	v_cvt_pk_bf16_f32 v26, v26, v27
	v_pk_mul_f32 v[10:11], v[16:17], s[14:15] op_sel_hi:[1,0]
	v_cvt_pk_bf16_f32 v27, v12, v13
	s_nop 0
	v_pk_mul_f32 v[12:13], v[14:15], s[14:15] op_sel_hi:[1,0]
	v_pk_mul_f32 v[14:15], v[22:23], s[14:15] op_sel_hi:[1,0]
	v_pk_mul_f32 v[16:17], v[20:21], s[14:15] op_sel_hi:[1,0]
	global_store_dwordx4 v[32:33], v[24:27], off
	v_lshl_add_u64 v[154:155], v[18:19], 0, v[174:175]
	s_waitcnt vmcnt(13)
	v_mov_b32_e32 v28, v192
	v_mov_b32_e32 v29, v193
	v_mov_b32_e32 v30, v194
	v_mov_b32_e32 v31, v195
	v_lshlrev_b32_e32 v20, 16, v28
	v_and_b32_e32 v21, 0xffff0000, v28
	v_lshlrev_b32_e32 v22, 16, v29
	v_and_b32_e32 v23, 0xffff0000, v29
	v_lshlrev_b32_e32 v24, 16, v30
	v_and_b32_e32 v25, 0xffff0000, v30
	v_lshlrev_b32_e32 v26, 16, v31
	v_and_b32_e32 v27, 0xffff0000, v31
	v_pk_fma_f32 v[22:23], v[148:149], v[10:11], v[22:23]
	v_pk_fma_f32 v[20:21], v[146:147], v[12:13], v[20:21]
	v_pk_fma_f32 v[26:27], v[144:145], v[14:15], v[26:27]
	v_pk_fma_f32 v[24:25], v[142:143], v[16:17], v[24:25]
	v_cvt_pk_bf16_f32 v20, v20, v21
	v_cvt_pk_bf16_f32 v21, v22, v23
	v_lshl_add_u64 v[28:29], v[18:19], 0, v[176:177]
	v_cvt_pk_bf16_f32 v22, v24, v25
	v_cvt_pk_bf16_f32 v23, v26, v27
	s_nop 0
	v_lshl_add_u64 v[30:31], v[18:19], 0, v[178:179]
	global_store_dwordx4 v[32:33], v[20:23], off offset:256
	s_waitcnt vmcnt(13)
	v_mov_b32_e32 v24, v204
	v_mov_b32_e32 v25, v205
	v_mov_b32_e32 v26, v206
	v_mov_b32_e32 v27, v207
	s_nop 0
	v_lshlrev_b32_e32 v20, 16, v24
	v_and_b32_e32 v21, 0xffff0000, v24
	v_lshlrev_b32_e32 v22, 16, v25
	v_and_b32_e32 v23, 0xffff0000, v25
	v_lshlrev_b32_e32 v24, 16, v26
	v_and_b32_e32 v25, 0xffff0000, v26
	v_lshlrev_b32_e32 v26, 16, v27
	v_and_b32_e32 v27, 0xffff0000, v27
	v_pk_fma_f32 v[22:23], v[152:153], v[8:9], v[22:23]
	v_pk_fma_f32 v[20:21], v[150:151], v[6:7], v[20:21]
	v_pk_fma_f32 v[26:27], v[140:141], v[4:5], v[26:27]
	v_pk_fma_f32 v[24:25], v[138:139], v[2:3], v[24:25]
	v_cvt_pk_bf16_f32 v20, v20, v21
	v_cvt_pk_bf16_f32 v21, v22, v23
	s_nop 0
	v_cvt_pk_bf16_f32 v22, v24, v25
	v_cvt_pk_bf16_f32 v23, v26, v27
	s_nop 0
	s_nop 0
	global_store_dwordx4 v[154:155], v[20:23], off
	s_waitcnt vmcnt(13)
	v_mov_b32_e32 v24, v208
	v_mov_b32_e32 v25, v209
	v_mov_b32_e32 v26, v210
	v_mov_b32_e32 v27, v211
	s_nop 0
	v_lshlrev_b32_e32 v20, 16, v24
	v_and_b32_e32 v21, 0xffff0000, v24
	v_lshlrev_b32_e32 v22, 16, v25
	v_and_b32_e32 v23, 0xffff0000, v25
	v_lshlrev_b32_e32 v24, 16, v26
	v_and_b32_e32 v25, 0xffff0000, v26
	v_lshlrev_b32_e32 v26, 16, v27
	v_and_b32_e32 v27, 0xffff0000, v27
	v_pk_fma_f32 v[22:23], v[132:133], v[10:11], v[22:23]
	v_pk_fma_f32 v[20:21], v[130:131], v[12:13], v[20:21]
	v_pk_fma_f32 v[26:27], v[128:129], v[14:15], v[26:27]
	v_pk_fma_f32 v[24:25], v[126:127], v[16:17], v[24:25]
	v_cvt_pk_bf16_f32 v20, v20, v21
	v_cvt_pk_bf16_f32 v21, v22, v23
	s_nop 0
	v_cvt_pk_bf16_f32 v22, v24, v25
	v_cvt_pk_bf16_f32 v23, v26, v27
	s_nop 0
	s_nop 0
	global_store_dwordx4 v[154:155], v[20:23], off offset:256
	s_waitcnt vmcnt(13)
	v_mov_b32_e32 v24, v212
	v_mov_b32_e32 v25, v213
	v_mov_b32_e32 v26, v214
	v_mov_b32_e32 v27, v215
	s_nop 0
	v_lshlrev_b32_e32 v20, 16, v24
	v_and_b32_e32 v21, 0xffff0000, v24
	v_lshlrev_b32_e32 v22, 16, v25
	v_and_b32_e32 v23, 0xffff0000, v25
	v_lshlrev_b32_e32 v24, 16, v26
	v_and_b32_e32 v25, 0xffff0000, v26
	v_lshlrev_b32_e32 v26, 16, v27
	v_and_b32_e32 v27, 0xffff0000, v27
	v_pk_fma_f32 v[22:23], v[136:137], v[8:9], v[22:23]
	v_pk_fma_f32 v[20:21], v[134:135], v[6:7], v[20:21]
	v_pk_fma_f32 v[26:27], v[124:125], v[4:5], v[26:27]
	v_pk_fma_f32 v[24:25], v[122:123], v[2:3], v[24:25]
	v_cvt_pk_bf16_f32 v20, v20, v21
	v_cvt_pk_bf16_f32 v21, v22, v23
	s_nop 0
	v_cvt_pk_bf16_f32 v22, v24, v25
	v_cvt_pk_bf16_f32 v23, v26, v27
	s_nop 0
	s_nop 0
	global_store_dwordx4 v[28:29], v[20:23], off
	s_waitcnt vmcnt(13)
	v_mov_b32_e32 v24, v216
	v_mov_b32_e32 v25, v217
	v_mov_b32_e32 v26, v218
	v_mov_b32_e32 v27, v219
	s_nop 0
	v_lshlrev_b32_e32 v20, 16, v24
	v_and_b32_e32 v21, 0xffff0000, v24
	v_lshlrev_b32_e32 v22, 16, v25
	v_and_b32_e32 v23, 0xffff0000, v25
	v_lshlrev_b32_e32 v24, 16, v26
	v_and_b32_e32 v25, 0xffff0000, v26
	v_lshlrev_b32_e32 v26, 16, v27
	v_and_b32_e32 v27, 0xffff0000, v27
	v_pk_fma_f32 v[22:23], v[116:117], v[10:11], v[22:23]
	v_pk_fma_f32 v[20:21], v[114:115], v[12:13], v[20:21]
	v_pk_fma_f32 v[26:27], v[112:113], v[14:15], v[26:27]
	v_pk_fma_f32 v[24:25], v[110:111], v[16:17], v[24:25]
	v_cvt_pk_bf16_f32 v20, v20, v21
	v_cvt_pk_bf16_f32 v21, v22, v23
	s_nop 0
	v_cvt_pk_bf16_f32 v22, v24, v25
	v_cvt_pk_bf16_f32 v23, v26, v27
	s_nop 0
	s_nop 0
	global_store_dwordx4 v[28:29], v[20:23], off offset:256
	v_lshl_add_u64 v[28:29], v[18:19], 0, v[180:181]
	s_waitcnt vmcnt(13)
	v_mov_b32_e32 v24, v220
	v_mov_b32_e32 v25, v221
	v_mov_b32_e32 v26, v222
	v_mov_b32_e32 v27, v223
	v_lshlrev_b32_e32 v20, 16, v24
	v_and_b32_e32 v21, 0xffff0000, v24
	v_lshlrev_b32_e32 v22, 16, v25
	v_and_b32_e32 v23, 0xffff0000, v25
	v_lshlrev_b32_e32 v24, 16, v26
	v_and_b32_e32 v25, 0xffff0000, v26
	v_lshlrev_b32_e32 v26, 16, v27
	v_and_b32_e32 v27, 0xffff0000, v27
	v_pk_fma_f32 v[22:23], v[120:121], v[8:9], v[22:23]
	v_pk_fma_f32 v[20:21], v[118:119], v[6:7], v[20:21]
	v_pk_fma_f32 v[26:27], v[108:109], v[4:5], v[26:27]
	v_pk_fma_f32 v[24:25], v[106:107], v[2:3], v[24:25]
	v_cvt_pk_bf16_f32 v20, v20, v21
	v_cvt_pk_bf16_f32 v21, v22, v23
	s_nop 0
	v_cvt_pk_bf16_f32 v22, v24, v25
	v_cvt_pk_bf16_f32 v23, v26, v27
	s_nop 0
	s_nop 0
	global_store_dwordx4 v[30:31], v[20:23], off
	s_waitcnt vmcnt(13)
	v_mov_b32_e32 v24, v224
	v_mov_b32_e32 v25, v225
	v_mov_b32_e32 v26, v226
	v_mov_b32_e32 v27, v227
	s_nop 0
	v_lshlrev_b32_e32 v20, 16, v24
	v_and_b32_e32 v21, 0xffff0000, v24
	v_lshlrev_b32_e32 v22, 16, v25
	v_and_b32_e32 v23, 0xffff0000, v25
	v_lshlrev_b32_e32 v24, 16, v26
	v_and_b32_e32 v25, 0xffff0000, v26
	v_lshlrev_b32_e32 v26, 16, v27
	v_and_b32_e32 v27, 0xffff0000, v27
	v_pk_fma_f32 v[22:23], v[104:105], v[10:11], v[22:23]
	v_pk_fma_f32 v[20:21], v[102:103], v[12:13], v[20:21]
	v_pk_fma_f32 v[26:27], v[100:101], v[14:15], v[26:27]
	v_pk_fma_f32 v[24:25], v[98:99], v[16:17], v[24:25]
	v_cvt_pk_bf16_f32 v20, v20, v21
	v_cvt_pk_bf16_f32 v21, v22, v23
	s_nop 0
	v_cvt_pk_bf16_f32 v22, v24, v25
	v_cvt_pk_bf16_f32 v23, v26, v27
	s_nop 0
	s_nop 0
	global_store_dwordx4 v[30:31], v[20:23], off offset:256
	v_lshl_add_u64 v[30:31], v[18:19], 0, v[182:183]
	s_waitcnt vmcnt(13)
	v_mov_b32_e32 v24, v228
	v_mov_b32_e32 v25, v229
	v_mov_b32_e32 v26, v230
	v_mov_b32_e32 v27, v231
	v_lshlrev_b32_e32 v20, 16, v24
	v_and_b32_e32 v21, 0xffff0000, v24
	v_lshlrev_b32_e32 v22, 16, v25
	v_and_b32_e32 v23, 0xffff0000, v25
	v_lshlrev_b32_e32 v24, 16, v26
	v_and_b32_e32 v25, 0xffff0000, v26
	v_lshlrev_b32_e32 v26, 16, v27
	v_and_b32_e32 v27, 0xffff0000, v27
	v_pk_fma_f32 v[22:23], v[96:97], v[8:9], v[22:23]
	v_pk_fma_f32 v[20:21], v[94:95], v[6:7], v[20:21]
	v_pk_fma_f32 v[26:27], v[92:93], v[4:5], v[26:27]
	v_pk_fma_f32 v[24:25], v[90:91], v[2:3], v[24:25]
	v_cvt_pk_bf16_f32 v20, v20, v21
	v_cvt_pk_bf16_f32 v21, v22, v23
	s_nop 0
	v_cvt_pk_bf16_f32 v22, v24, v25
	v_cvt_pk_bf16_f32 v23, v26, v27
	s_nop 0
	s_nop 0
	global_store_dwordx4 v[28:29], v[20:23], off
	s_waitcnt vmcnt(13)
	v_mov_b32_e32 v24, v232
	v_mov_b32_e32 v25, v233
	v_mov_b32_e32 v26, v234
	v_mov_b32_e32 v27, v235
	s_nop 0
	v_lshlrev_b32_e32 v20, 16, v24
	v_and_b32_e32 v21, 0xffff0000, v24
	v_lshlrev_b32_e32 v22, 16, v25
	v_and_b32_e32 v23, 0xffff0000, v25
	v_lshlrev_b32_e32 v24, 16, v26
	v_and_b32_e32 v25, 0xffff0000, v26
	v_lshlrev_b32_e32 v26, 16, v27
	v_and_b32_e32 v27, 0xffff0000, v27
	v_pk_fma_f32 v[22:23], v[84:85], v[10:11], v[22:23]
	v_pk_fma_f32 v[20:21], v[82:83], v[12:13], v[20:21]
	v_pk_fma_f32 v[26:27], v[80:81], v[14:15], v[26:27]
	v_pk_fma_f32 v[24:25], v[78:79], v[16:17], v[24:25]
	v_cvt_pk_bf16_f32 v20, v20, v21
	v_cvt_pk_bf16_f32 v21, v22, v23
	s_nop 0
	v_cvt_pk_bf16_f32 v22, v24, v25
	v_cvt_pk_bf16_f32 v23, v26, v27
	s_nop 0
	s_nop 0
	global_store_dwordx4 v[28:29], v[20:23], off offset:256
	v_lshl_add_u64 v[28:29], v[18:19], 0, v[184:185]
	s_waitcnt vmcnt(13)
	v_mov_b32_e32 v24, v236
	v_mov_b32_e32 v25, v237
	v_mov_b32_e32 v26, v238
	v_mov_b32_e32 v27, v239
	v_lshlrev_b32_e32 v20, 16, v24
	v_and_b32_e32 v21, 0xffff0000, v24
	v_lshlrev_b32_e32 v22, 16, v25
	v_and_b32_e32 v23, 0xffff0000, v25
	v_lshlrev_b32_e32 v24, 16, v26
	v_and_b32_e32 v25, 0xffff0000, v26
	v_lshlrev_b32_e32 v26, 16, v27
	v_and_b32_e32 v27, 0xffff0000, v27
	v_pk_fma_f32 v[22:23], v[88:89], v[8:9], v[22:23]
	v_pk_fma_f32 v[20:21], v[86:87], v[6:7], v[20:21]
	v_pk_fma_f32 v[26:27], v[76:77], v[4:5], v[26:27]
	v_pk_fma_f32 v[24:25], v[74:75], v[2:3], v[24:25]
	v_cvt_pk_bf16_f32 v20, v20, v21
	v_cvt_pk_bf16_f32 v21, v22, v23
	s_nop 0
	v_cvt_pk_bf16_f32 v22, v24, v25
	v_cvt_pk_bf16_f32 v23, v26, v27
	s_nop 0
	s_nop 0
	global_store_dwordx4 v[30:31], v[20:23], off
	s_waitcnt vmcnt(13)
	v_mov_b32_e32 v24, v240
	v_mov_b32_e32 v25, v241
	v_mov_b32_e32 v26, v242
	v_mov_b32_e32 v27, v243
	s_nop 0
	v_lshlrev_b32_e32 v20, 16, v24
	v_and_b32_e32 v21, 0xffff0000, v24
	v_lshlrev_b32_e32 v22, 16, v25
	v_and_b32_e32 v23, 0xffff0000, v25
	v_lshlrev_b32_e32 v24, 16, v26
	v_and_b32_e32 v25, 0xffff0000, v26
	v_lshlrev_b32_e32 v26, 16, v27
	v_and_b32_e32 v27, 0xffff0000, v27
	v_pk_fma_f32 v[22:23], v[68:69], v[10:11], v[22:23]
	v_pk_fma_f32 v[20:21], v[66:67], v[12:13], v[20:21]
	v_pk_fma_f32 v[26:27], v[64:65], v[14:15], v[26:27]
	v_pk_fma_f32 v[24:25], v[62:63], v[16:17], v[24:25]
	v_cvt_pk_bf16_f32 v20, v20, v21
	v_cvt_pk_bf16_f32 v21, v22, v23
	s_nop 0
	v_cvt_pk_bf16_f32 v22, v24, v25
	v_cvt_pk_bf16_f32 v23, v26, v27
	s_nop 0
	s_nop 0
	global_store_dwordx4 v[30:31], v[20:23], off offset:256
	v_lshl_add_u64 v[30:31], v[18:19], 0, v[186:187]
	s_waitcnt vmcnt(13)
	v_mov_b32_e32 v24, v244
	v_mov_b32_e32 v25, v245
	v_mov_b32_e32 v26, v246
	v_mov_b32_e32 v27, v247
	v_lshlrev_b32_e32 v20, 16, v24
	v_and_b32_e32 v21, 0xffff0000, v24
	v_lshlrev_b32_e32 v22, 16, v25
	v_and_b32_e32 v23, 0xffff0000, v25
	v_lshlrev_b32_e32 v24, 16, v26
	v_and_b32_e32 v25, 0xffff0000, v26
	v_lshlrev_b32_e32 v26, 16, v27
	v_and_b32_e32 v27, 0xffff0000, v27
	v_pk_fma_f32 v[22:23], v[72:73], v[8:9], v[22:23]
	v_pk_fma_f32 v[20:21], v[70:71], v[6:7], v[20:21]
	v_pk_fma_f32 v[26:27], v[60:61], v[4:5], v[26:27]
	v_pk_fma_f32 v[24:25], v[58:59], v[2:3], v[24:25]
	v_cvt_pk_bf16_f32 v20, v20, v21
	v_cvt_pk_bf16_f32 v21, v22, v23
	s_nop 0
	v_cvt_pk_bf16_f32 v22, v24, v25
	v_cvt_pk_bf16_f32 v23, v26, v27
	s_nop 0
	s_waitcnt vmcnt(12)
	v_mov_b32_e32 v24, v248
	v_mov_b32_e32 v25, v249
	v_mov_b32_e32 v26, v250
	v_mov_b32_e32 v27, v251
	v_lshlrev_b32_e32 v18, 16, v24
	global_store_dwordx4 v[28:29], v[20:23], off
	v_and_b32_e32 v19, 0xffff0000, v24
	v_lshlrev_b32_e32 v24, 16, v27
	v_lshlrev_b32_e32 v20, 16, v25
	v_and_b32_e32 v21, 0xffff0000, v25
	v_lshlrev_b32_e32 v22, 16, v26
	v_and_b32_e32 v23, 0xffff0000, v26
	v_and_b32_e32 v25, 0xffff0000, v27
	v_pk_fma_f32 v[20:21], v[52:53], v[10:11], v[20:21]
	v_pk_fma_f32 v[18:19], v[50:51], v[12:13], v[18:19]
	v_pk_fma_f32 v[24:25], v[48:49], v[14:15], v[24:25]
	v_pk_fma_f32 v[22:23], v[46:47], v[16:17], v[22:23]
	v_cvt_pk_bf16_f32 v18, v18, v19
	v_cvt_pk_bf16_f32 v19, v20, v21
	s_nop 0
	v_cvt_pk_bf16_f32 v20, v22, v23
	v_cvt_pk_bf16_f32 v21, v24, v25
	global_load_dwordx4 v[22:25], v[30:31], off
	s_nop 0
	global_store_dwordx4 v[28:29], v[18:21], off offset:256
	s_waitcnt vmcnt(1)
	s_nop 0
	v_lshlrev_b32_e32 v18, 16, v22
	v_and_b32_e32 v19, 0xffff0000, v22
	v_lshlrev_b32_e32 v20, 16, v23
	v_and_b32_e32 v21, 0xffff0000, v23
	v_lshlrev_b32_e32 v22, 16, v24
	v_and_b32_e32 v23, 0xffff0000, v24
	v_lshlrev_b32_e32 v24, 16, v25
	v_and_b32_e32 v25, 0xffff0000, v25
	v_pk_fma_f32 v[8:9], v[56:57], v[8:9], v[20:21]
	v_pk_fma_f32 v[6:7], v[54:55], v[6:7], v[18:19]
	v_pk_fma_f32 v[18:19], v[44:45], v[4:5], v[24:25]
	v_pk_fma_f32 v[4:5], v[42:43], v[2:3], v[22:23]
	v_cvt_pk_bf16_f32 v2, v6, v7
	v_cvt_pk_bf16_f32 v3, v8, v9
	s_nop 0
	v_cvt_pk_bf16_f32 v4, v4, v5
	v_cvt_pk_bf16_f32 v5, v18, v19
	global_load_dwordx4 v[6:9], v[30:31], off offset:256
	s_nop 0
	global_store_dwordx4 v[30:31], v[2:5], off
	s_waitcnt vmcnt(1)
	s_nop 0
	v_lshlrev_b32_e32 v2, 16, v6
	v_and_b32_e32 v3, 0xffff0000, v6
	v_lshlrev_b32_e32 v4, 16, v7
	v_and_b32_e32 v5, 0xffff0000, v7
	v_lshlrev_b32_e32 v6, 16, v8
	v_and_b32_e32 v7, 0xffff0000, v8
	v_lshlrev_b32_e32 v8, 16, v9
	v_and_b32_e32 v9, 0xffff0000, v9
	v_pk_fma_f32 v[4:5], v[40:41], v[10:11], v[4:5]
	v_pk_fma_f32 v[2:3], v[38:39], v[12:13], v[2:3]
	v_pk_fma_f32 v[8:9], v[36:37], v[14:15], v[8:9]
	v_pk_fma_f32 v[6:7], v[34:35], v[16:17], v[6:7]
	v_cvt_pk_bf16_f32 v2, v2, v3
	v_cvt_pk_bf16_f32 v3, v4, v5
	s_nop 0
	v_cvt_pk_bf16_f32 v4, v6, v7
	v_cvt_pk_bf16_f32 v5, v8, v9
	global_store_dwordx4 v[30:31], v[2:5], off offset:256
	s_cbranch_vccnz .LBB0_1527
	s_andn2_b64 vcc, exec, s[2:3]
	s_cbranch_vccnz .LBB0_1526
	s_barrier
	s_branch .LBB0_1526

.LBB0_2353:
	s_ashr_i32 s13, s20, 3
	s_mul_hi_i32 s15, s13, 0xc000
	s_mul_i32 s13, s13, 0xc000
	s_add_u32 s22, s39, s13
	s_addc_u32 s23, s40, s15
	s_ashr_i32 s21, s20, 31
	s_lshl_b64 s[20:21], s[20:21], 20
	v_lshl_or_b32 v10, s48, 8, v200
	s_add_u32 s20, s41, s20
	v_ashrrev_i32_e32 v11, 31, v10
	s_nop 15
	s_nop 15
	v_lshl_add_u64 v[14:15], v[10:11], 2, s[22:23]
	s_addc_u32 s21, s42, s21
	global_load_dwordx4 v[2:5], v[14:15], off offset:16
	global_load_dwordx4 v[6:9], v[14:15], off
	v_lshl_add_u64 v[18:19], v[10:11], 1, s[20:21]
	v_lshl_add_u64 v[32:33], v[18:19], 0, v[172:173]
	global_load_dwordx4 v[10:13], v[32:33], off
	global_load_dwordx4 v[20:23], v[14:15], off offset:528
	s_nop 0
	global_load_dwordx4 v[14:17], v[14:15], off offset:512
	s_andn2_b64 vcc, exec, s[6:7]
	s_mov_b64 s[6:7], -1
	v_lshl_add_u64 v[252:253], v[18:19], 0, v[172:173]
	global_load_dwordx4 v[192:195], v[252:253], off offset:256
	v_lshl_add_u64 v[252:253], v[18:19], 0, v[174:175]
	global_load_dwordx4 v[204:207], v[252:253], off
	global_load_dwordx4 v[208:211], v[252:253], off offset:256
	v_lshl_add_u64 v[252:253], v[18:19], 0, v[176:177]
	global_load_dwordx4 v[212:215], v[252:253], off
	global_load_dwordx4 v[216:219], v[252:253], off offset:256
	v_lshl_add_u64 v[252:253], v[18:19], 0, v[178:179]
	global_load_dwordx4 v[220:223], v[252:253], off
	global_load_dwordx4 v[224:227], v[252:253], off offset:256
	v_lshl_add_u64 v[252:253], v[18:19], 0, v[180:181]
	global_load_dwordx4 v[228:231], v[252:253], off
	global_load_dwordx4 v[232:235], v[252:253], off offset:256
	v_lshl_add_u64 v[252:253], v[18:19], 0, v[182:183]
	global_load_dwordx4 v[236:239], v[252:253], off
	global_load_dwordx4 v[240:243], v[252:253], off offset:256
	v_lshl_add_u64 v[252:253], v[18:19], 0, v[184:185]
	global_load_dwordx4 v[244:247], v[252:253], off
	global_load_dwordx4 v[248:251], v[252:253], off offset:256
	s_waitcnt vmcnt(13)
	v_pk_mul_f32 v[2:3], v[2:3], s[10:11] op_sel_hi:[1,0]
	v_pk_mul_f32 v[6:7], v[6:7], s[10:11] op_sel_hi:[1,0]
	v_lshlrev_b32_e32 v24, 16, v10
	v_and_b32_e32 v25, 0xffff0000, v10
	v_lshlrev_b32_e32 v26, 16, v12
	v_and_b32_e32 v27, 0xffff0000, v12
	v_pk_mul_f32 v[8:9], v[8:9], s[10:11] op_sel_hi:[1,0]
	v_pk_mul_f32 v[4:5], v[4:5], s[10:11] op_sel_hi:[1,0]
	v_lshlrev_b32_e32 v10, 16, v11
	v_and_b32_e32 v11, 0xffff0000, v11
	v_lshlrev_b32_e32 v12, 16, v13
	v_and_b32_e32 v13, 0xffff0000, v13
	v_pk_fma_f32 v[24:25], v[158:159], v[6:7], v[24:25]
	v_pk_fma_f32 v[26:27], v[154:155], v[2:3], v[26:27]
	v_pk_fma_f32 v[10:11], v[160:161], v[8:9], v[10:11]
	v_pk_fma_f32 v[12:13], v[156:157], v[4:5], v[12:13]
	v_cvt_pk_bf16_f32 v24, v24, v25
	v_cvt_pk_bf16_f32 v25, v10, v11
	v_cvt_pk_bf16_f32 v26, v26, v27
	v_pk_mul_f32 v[10:11], v[16:17], s[10:11] op_sel_hi:[1,0]
	v_cvt_pk_bf16_f32 v27, v12, v13
	s_nop 0
	v_pk_mul_f32 v[12:13], v[14:15], s[10:11] op_sel_hi:[1,0]
	v_pk_mul_f32 v[14:15], v[22:23], s[10:11] op_sel_hi:[1,0]
	v_pk_mul_f32 v[16:17], v[20:21], s[10:11] op_sel_hi:[1,0]
	global_store_dwordx4 v[32:33], v[24:27], off
	v_lshl_add_u64 v[154:155], v[18:19], 0, v[174:175]
	s_waitcnt vmcnt(13)
	v_mov_b32_e32 v28, v192
	v_mov_b32_e32 v29, v193
	v_mov_b32_e32 v30, v194
	v_mov_b32_e32 v31, v195
	v_lshlrev_b32_e32 v20, 16, v28
	v_and_b32_e32 v21, 0xffff0000, v28
	v_lshlrev_b32_e32 v22, 16, v29
	v_and_b32_e32 v23, 0xffff0000, v29
	v_lshlrev_b32_e32 v24, 16, v30
	v_and_b32_e32 v25, 0xffff0000, v30
	v_lshlrev_b32_e32 v26, 16, v31
	v_and_b32_e32 v27, 0xffff0000, v31
	v_pk_fma_f32 v[22:23], v[148:149], v[10:11], v[22:23]
	v_pk_fma_f32 v[20:21], v[146:147], v[12:13], v[20:21]
	v_pk_fma_f32 v[26:27], v[144:145], v[14:15], v[26:27]
	v_pk_fma_f32 v[24:25], v[142:143], v[16:17], v[24:25]
	v_cvt_pk_bf16_f32 v20, v20, v21
	v_cvt_pk_bf16_f32 v21, v22, v23
	v_lshl_add_u64 v[28:29], v[18:19], 0, v[176:177]
	v_cvt_pk_bf16_f32 v22, v24, v25
	v_cvt_pk_bf16_f32 v23, v26, v27
	s_nop 0
	v_lshl_add_u64 v[30:31], v[18:19], 0, v[178:179]
	global_store_dwordx4 v[32:33], v[20:23], off offset:256
	s_waitcnt vmcnt(13)
	v_mov_b32_e32 v24, v204
	v_mov_b32_e32 v25, v205
	v_mov_b32_e32 v26, v206
	v_mov_b32_e32 v27, v207
	s_nop 0
	v_lshlrev_b32_e32 v20, 16, v24
	v_and_b32_e32 v21, 0xffff0000, v24
	v_lshlrev_b32_e32 v22, 16, v25
	v_and_b32_e32 v23, 0xffff0000, v25
	v_lshlrev_b32_e32 v24, 16, v26
	v_and_b32_e32 v25, 0xffff0000, v26
	v_lshlrev_b32_e32 v26, 16, v27
	v_and_b32_e32 v27, 0xffff0000, v27
	v_pk_fma_f32 v[22:23], v[152:153], v[8:9], v[22:23]
	v_pk_fma_f32 v[20:21], v[150:151], v[6:7], v[20:21]
	v_pk_fma_f32 v[26:27], v[140:141], v[4:5], v[26:27]
	v_pk_fma_f32 v[24:25], v[138:139], v[2:3], v[24:25]
	v_cvt_pk_bf16_f32 v20, v20, v21
	v_cvt_pk_bf16_f32 v21, v22, v23
	s_nop 0
	v_cvt_pk_bf16_f32 v22, v24, v25
	v_cvt_pk_bf16_f32 v23, v26, v27
	s_nop 0
	s_nop 0
	global_store_dwordx4 v[154:155], v[20:23], off
	s_waitcnt vmcnt(13)
	v_mov_b32_e32 v24, v208
	v_mov_b32_e32 v25, v209
	v_mov_b32_e32 v26, v210
	v_mov_b32_e32 v27, v211
	s_nop 0
	v_lshlrev_b32_e32 v20, 16, v24
	v_and_b32_e32 v21, 0xffff0000, v24
	v_lshlrev_b32_e32 v22, 16, v25
	v_and_b32_e32 v23, 0xffff0000, v25
	v_lshlrev_b32_e32 v24, 16, v26
	v_and_b32_e32 v25, 0xffff0000, v26
	v_lshlrev_b32_e32 v26, 16, v27
	v_and_b32_e32 v27, 0xffff0000, v27
	v_pk_fma_f32 v[22:23], v[132:133], v[10:11], v[22:23]
	v_pk_fma_f32 v[20:21], v[130:131], v[12:13], v[20:21]
	v_pk_fma_f32 v[26:27], v[128:129], v[14:15], v[26:27]
	v_pk_fma_f32 v[24:25], v[126:127], v[16:17], v[24:25]
	v_cvt_pk_bf16_f32 v20, v20, v21
	v_cvt_pk_bf16_f32 v21, v22, v23
	s_nop 0
	v_cvt_pk_bf16_f32 v22, v24, v25
	v_cvt_pk_bf16_f32 v23, v26, v27
	s_nop 0
	s_nop 0
	global_store_dwordx4 v[154:155], v[20:23], off offset:256
	s_waitcnt vmcnt(13)
	v_mov_b32_e32 v24, v212
	v_mov_b32_e32 v25, v213
	v_mov_b32_e32 v26, v214
	v_mov_b32_e32 v27, v215
	s_nop 0
	v_lshlrev_b32_e32 v20, 16, v24
	v_and_b32_e32 v21, 0xffff0000, v24
	v_lshlrev_b32_e32 v22, 16, v25
	v_and_b32_e32 v23, 0xffff0000, v25
	v_lshlrev_b32_e32 v24, 16, v26
	v_and_b32_e32 v25, 0xffff0000, v26
	v_lshlrev_b32_e32 v26, 16, v27
	v_and_b32_e32 v27, 0xffff0000, v27
	v_pk_fma_f32 v[22:23], v[136:137], v[8:9], v[22:23]
	v_pk_fma_f32 v[20:21], v[134:135], v[6:7], v[20:21]
	v_pk_fma_f32 v[26:27], v[124:125], v[4:5], v[26:27]
	v_pk_fma_f32 v[24:25], v[122:123], v[2:3], v[24:25]
	v_cvt_pk_bf16_f32 v20, v20, v21
	v_cvt_pk_bf16_f32 v21, v22, v23
	s_nop 0
	v_cvt_pk_bf16_f32 v22, v24, v25
	v_cvt_pk_bf16_f32 v23, v26, v27
	s_nop 0
	s_nop 0
	global_store_dwordx4 v[28:29], v[20:23], off
	s_waitcnt vmcnt(13)
	v_mov_b32_e32 v24, v216
	v_mov_b32_e32 v25, v217
	v_mov_b32_e32 v26, v218
	v_mov_b32_e32 v27, v219
	s_nop 0
	v_lshlrev_b32_e32 v20, 16, v24
	v_and_b32_e32 v21, 0xffff0000, v24
	v_lshlrev_b32_e32 v22, 16, v25
	v_and_b32_e32 v23, 0xffff0000, v25
	v_lshlrev_b32_e32 v24, 16, v26
	v_and_b32_e32 v25, 0xffff0000, v26
	v_lshlrev_b32_e32 v26, 16, v27
	v_and_b32_e32 v27, 0xffff0000, v27
	v_pk_fma_f32 v[22:23], v[116:117], v[10:11], v[22:23]
	v_pk_fma_f32 v[20:21], v[114:115], v[12:13], v[20:21]
	v_pk_fma_f32 v[26:27], v[112:113], v[14:15], v[26:27]
	v_pk_fma_f32 v[24:25], v[110:111], v[16:17], v[24:25]
	v_cvt_pk_bf16_f32 v20, v20, v21
	v_cvt_pk_bf16_f32 v21, v22, v23
	s_nop 0
	v_cvt_pk_bf16_f32 v22, v24, v25
	v_cvt_pk_bf16_f32 v23, v26, v27
	s_nop 0
	s_nop 0
	global_store_dwordx4 v[28:29], v[20:23], off offset:256
	v_lshl_add_u64 v[28:29], v[18:19], 0, v[180:181]
	s_waitcnt vmcnt(13)
	v_mov_b32_e32 v24, v220
	v_mov_b32_e32 v25, v221
	v_mov_b32_e32 v26, v222
	v_mov_b32_e32 v27, v223
	v_lshlrev_b32_e32 v20, 16, v24
	v_and_b32_e32 v21, 0xffff0000, v24
	v_lshlrev_b32_e32 v22, 16, v25
	v_and_b32_e32 v23, 0xffff0000, v25
	v_lshlrev_b32_e32 v24, 16, v26
	v_and_b32_e32 v25, 0xffff0000, v26
	v_lshlrev_b32_e32 v26, 16, v27
	v_and_b32_e32 v27, 0xffff0000, v27
	v_pk_fma_f32 v[22:23], v[120:121], v[8:9], v[22:23]
	v_pk_fma_f32 v[20:21], v[118:119], v[6:7], v[20:21]
	v_pk_fma_f32 v[26:27], v[108:109], v[4:5], v[26:27]
	v_pk_fma_f32 v[24:25], v[106:107], v[2:3], v[24:25]
	v_cvt_pk_bf16_f32 v20, v20, v21
	v_cvt_pk_bf16_f32 v21, v22, v23
	s_nop 0
	v_cvt_pk_bf16_f32 v22, v24, v25
	v_cvt_pk_bf16_f32 v23, v26, v27
	s_nop 0
	s_nop 0
	global_store_dwordx4 v[30:31], v[20:23], off
	s_waitcnt vmcnt(13)
	v_mov_b32_e32 v24, v224
	v_mov_b32_e32 v25, v225
	v_mov_b32_e32 v26, v226
	v_mov_b32_e32 v27, v227
	s_nop 0
	v_lshlrev_b32_e32 v20, 16, v24
	v_and_b32_e32 v21, 0xffff0000, v24
	v_lshlrev_b32_e32 v22, 16, v25
	v_and_b32_e32 v23, 0xffff0000, v25
	v_lshlrev_b32_e32 v24, 16, v26
	v_and_b32_e32 v25, 0xffff0000, v26
	v_lshlrev_b32_e32 v26, 16, v27
	v_and_b32_e32 v27, 0xffff0000, v27
	v_pk_fma_f32 v[22:23], v[104:105], v[10:11], v[22:23]
	v_pk_fma_f32 v[20:21], v[102:103], v[12:13], v[20:21]
	v_pk_fma_f32 v[26:27], v[100:101], v[14:15], v[26:27]
	v_pk_fma_f32 v[24:25], v[98:99], v[16:17], v[24:25]
	v_cvt_pk_bf16_f32 v20, v20, v21
	v_cvt_pk_bf16_f32 v21, v22, v23
	s_nop 0
	v_cvt_pk_bf16_f32 v22, v24, v25
	v_cvt_pk_bf16_f32 v23, v26, v27
	s_nop 0
	s_nop 0
	global_store_dwordx4 v[30:31], v[20:23], off offset:256
	v_lshl_add_u64 v[30:31], v[18:19], 0, v[182:183]
	s_waitcnt vmcnt(13)
	v_mov_b32_e32 v24, v228
	v_mov_b32_e32 v25, v229
	v_mov_b32_e32 v26, v230
	v_mov_b32_e32 v27, v231
	v_lshlrev_b32_e32 v20, 16, v24
	v_and_b32_e32 v21, 0xffff0000, v24
	v_lshlrev_b32_e32 v22, 16, v25
	v_and_b32_e32 v23, 0xffff0000, v25
	v_lshlrev_b32_e32 v24, 16, v26
	v_and_b32_e32 v25, 0xffff0000, v26
	v_lshlrev_b32_e32 v26, 16, v27
	v_and_b32_e32 v27, 0xffff0000, v27
	v_pk_fma_f32 v[22:23], v[96:97], v[8:9], v[22:23]
	v_pk_fma_f32 v[20:21], v[94:95], v[6:7], v[20:21]
	v_pk_fma_f32 v[26:27], v[92:93], v[4:5], v[26:27]
	v_pk_fma_f32 v[24:25], v[90:91], v[2:3], v[24:25]
	v_cvt_pk_bf16_f32 v20, v20, v21
	v_cvt_pk_bf16_f32 v21, v22, v23
	s_nop 0
	v_cvt_pk_bf16_f32 v22, v24, v25
	v_cvt_pk_bf16_f32 v23, v26, v27
	s_nop 0
	s_nop 0
	global_store_dwordx4 v[28:29], v[20:23], off
	s_waitcnt vmcnt(13)
	v_mov_b32_e32 v24, v232
	v_mov_b32_e32 v25, v233
	v_mov_b32_e32 v26, v234
	v_mov_b32_e32 v27, v235
	s_nop 0
	v_lshlrev_b32_e32 v20, 16, v24
	v_and_b32_e32 v21, 0xffff0000, v24
	v_lshlrev_b32_e32 v22, 16, v25
	v_and_b32_e32 v23, 0xffff0000, v25
	v_lshlrev_b32_e32 v24, 16, v26
	v_and_b32_e32 v25, 0xffff0000, v26
	v_lshlrev_b32_e32 v26, 16, v27
	v_and_b32_e32 v27, 0xffff0000, v27
	v_pk_fma_f32 v[22:23], v[84:85], v[10:11], v[22:23]
	v_pk_fma_f32 v[20:21], v[82:83], v[12:13], v[20:21]
	v_pk_fma_f32 v[26:27], v[80:81], v[14:15], v[26:27]
	v_pk_fma_f32 v[24:25], v[78:79], v[16:17], v[24:25]
	v_cvt_pk_bf16_f32 v20, v20, v21
	v_cvt_pk_bf16_f32 v21, v22, v23
	s_nop 0
	v_cvt_pk_bf16_f32 v22, v24, v25
	v_cvt_pk_bf16_f32 v23, v26, v27
	s_nop 0
	s_nop 0
	global_store_dwordx4 v[28:29], v[20:23], off offset:256
	v_lshl_add_u64 v[28:29], v[18:19], 0, v[184:185]
	s_waitcnt vmcnt(13)
	v_mov_b32_e32 v24, v236
	v_mov_b32_e32 v25, v237
	v_mov_b32_e32 v26, v238
	v_mov_b32_e32 v27, v239
	v_lshlrev_b32_e32 v20, 16, v24
	v_and_b32_e32 v21, 0xffff0000, v24
	v_lshlrev_b32_e32 v22, 16, v25
	v_and_b32_e32 v23, 0xffff0000, v25
	v_lshlrev_b32_e32 v24, 16, v26
	v_and_b32_e32 v25, 0xffff0000, v26
	v_lshlrev_b32_e32 v26, 16, v27
	v_and_b32_e32 v27, 0xffff0000, v27
	v_pk_fma_f32 v[22:23], v[88:89], v[8:9], v[22:23]
	v_pk_fma_f32 v[20:21], v[86:87], v[6:7], v[20:21]
	v_pk_fma_f32 v[26:27], v[76:77], v[4:5], v[26:27]
	v_pk_fma_f32 v[24:25], v[74:75], v[2:3], v[24:25]
	v_cvt_pk_bf16_f32 v20, v20, v21
	v_cvt_pk_bf16_f32 v21, v22, v23
	s_nop 0
	v_cvt_pk_bf16_f32 v22, v24, v25
	v_cvt_pk_bf16_f32 v23, v26, v27
	s_nop 0
	s_nop 0
	global_store_dwordx4 v[30:31], v[20:23], off
	s_waitcnt vmcnt(13)
	v_mov_b32_e32 v24, v240
	v_mov_b32_e32 v25, v241
	v_mov_b32_e32 v26, v242
	v_mov_b32_e32 v27, v243
	s_nop 0
	v_lshlrev_b32_e32 v20, 16, v24
	v_and_b32_e32 v21, 0xffff0000, v24
	v_lshlrev_b32_e32 v22, 16, v25
	v_and_b32_e32 v23, 0xffff0000, v25
	v_lshlrev_b32_e32 v24, 16, v26
	v_and_b32_e32 v25, 0xffff0000, v26
	v_lshlrev_b32_e32 v26, 16, v27
	v_and_b32_e32 v27, 0xffff0000, v27
	v_pk_fma_f32 v[22:23], v[68:69], v[10:11], v[22:23]
	v_pk_fma_f32 v[20:21], v[66:67], v[12:13], v[20:21]
	v_pk_fma_f32 v[26:27], v[64:65], v[14:15], v[26:27]
	v_pk_fma_f32 v[24:25], v[62:63], v[16:17], v[24:25]
	v_cvt_pk_bf16_f32 v20, v20, v21
	v_cvt_pk_bf16_f32 v21, v22, v23
	s_nop 0
	v_cvt_pk_bf16_f32 v22, v24, v25
	v_cvt_pk_bf16_f32 v23, v26, v27
	s_nop 0
	s_nop 0
	global_store_dwordx4 v[30:31], v[20:23], off offset:256
	v_lshl_add_u64 v[30:31], v[18:19], 0, v[186:187]
	s_waitcnt vmcnt(13)
	v_mov_b32_e32 v24, v244
	v_mov_b32_e32 v25, v245
	v_mov_b32_e32 v26, v246
	v_mov_b32_e32 v27, v247
	v_lshlrev_b32_e32 v20, 16, v24
	v_and_b32_e32 v21, 0xffff0000, v24
	v_lshlrev_b32_e32 v22, 16, v25
	v_and_b32_e32 v23, 0xffff0000, v25
	v_lshlrev_b32_e32 v24, 16, v26
	v_and_b32_e32 v25, 0xffff0000, v26
	v_lshlrev_b32_e32 v26, 16, v27
	v_and_b32_e32 v27, 0xffff0000, v27
	v_pk_fma_f32 v[22:23], v[72:73], v[8:9], v[22:23]
	v_pk_fma_f32 v[20:21], v[70:71], v[6:7], v[20:21]
	v_pk_fma_f32 v[26:27], v[60:61], v[4:5], v[26:27]
	v_pk_fma_f32 v[24:25], v[58:59], v[2:3], v[24:25]
	v_cvt_pk_bf16_f32 v20, v20, v21
	v_cvt_pk_bf16_f32 v21, v22, v23
	s_nop 0
	v_cvt_pk_bf16_f32 v22, v24, v25
	v_cvt_pk_bf16_f32 v23, v26, v27
	s_nop 0
	s_waitcnt vmcnt(12)
	v_mov_b32_e32 v24, v248
	v_mov_b32_e32 v25, v249
	v_mov_b32_e32 v26, v250
	v_mov_b32_e32 v27, v251
	v_lshlrev_b32_e32 v18, 16, v24
	global_store_dwordx4 v[28:29], v[20:23], off
	v_and_b32_e32 v19, 0xffff0000, v24
	v_lshlrev_b32_e32 v24, 16, v27
	v_lshlrev_b32_e32 v20, 16, v25
	v_and_b32_e32 v21, 0xffff0000, v25
	v_lshlrev_b32_e32 v22, 16, v26
	v_and_b32_e32 v23, 0xffff0000, v26
	v_and_b32_e32 v25, 0xffff0000, v27
	v_pk_fma_f32 v[20:21], v[52:53], v[10:11], v[20:21]
	v_pk_fma_f32 v[18:19], v[50:51], v[12:13], v[18:19]
	v_pk_fma_f32 v[24:25], v[48:49], v[14:15], v[24:25]
	v_pk_fma_f32 v[22:23], v[46:47], v[16:17], v[22:23]
	v_cvt_pk_bf16_f32 v18, v18, v19
	v_cvt_pk_bf16_f32 v19, v20, v21
	s_nop 0
	v_cvt_pk_bf16_f32 v20, v22, v23
	v_cvt_pk_bf16_f32 v21, v24, v25
	global_load_dwordx4 v[22:25], v[30:31], off
	s_nop 0
	global_store_dwordx4 v[28:29], v[18:21], off offset:256
	s_waitcnt vmcnt(1)
	s_nop 0
	v_lshlrev_b32_e32 v18, 16, v22
	v_and_b32_e32 v19, 0xffff0000, v22
	v_lshlrev_b32_e32 v20, 16, v23
	v_and_b32_e32 v21, 0xffff0000, v23
	v_lshlrev_b32_e32 v22, 16, v24
	v_and_b32_e32 v23, 0xffff0000, v24
	v_lshlrev_b32_e32 v24, 16, v25
	v_and_b32_e32 v25, 0xffff0000, v25
	v_pk_fma_f32 v[8:9], v[56:57], v[8:9], v[20:21]
	v_pk_fma_f32 v[6:7], v[54:55], v[6:7], v[18:19]
	v_pk_fma_f32 v[18:19], v[44:45], v[4:5], v[24:25]
	v_pk_fma_f32 v[4:5], v[42:43], v[2:3], v[22:23]
	v_cvt_pk_bf16_f32 v2, v6, v7
	v_cvt_pk_bf16_f32 v3, v8, v9
	s_nop 0
	v_cvt_pk_bf16_f32 v4, v4, v5
	v_cvt_pk_bf16_f32 v5, v18, v19
	global_load_dwordx4 v[6:9], v[30:31], off offset:256
	s_nop 0
	global_store_dwordx4 v[30:31], v[2:5], off
	s_waitcnt vmcnt(1)
	s_nop 0
	v_lshlrev_b32_e32 v2, 16, v6
	v_and_b32_e32 v3, 0xffff0000, v6
	v_lshlrev_b32_e32 v4, 16, v7
	v_and_b32_e32 v5, 0xffff0000, v7
	v_lshlrev_b32_e32 v6, 16, v8
	v_and_b32_e32 v7, 0xffff0000, v8
	v_lshlrev_b32_e32 v8, 16, v9
	v_and_b32_e32 v9, 0xffff0000, v9
	v_pk_fma_f32 v[4:5], v[40:41], v[10:11], v[4:5]
	v_pk_fma_f32 v[2:3], v[38:39], v[12:13], v[2:3]
	v_pk_fma_f32 v[8:9], v[36:37], v[14:15], v[8:9]
	v_pk_fma_f32 v[6:7], v[34:35], v[16:17], v[6:7]
	v_cvt_pk_bf16_f32 v2, v2, v3
	v_cvt_pk_bf16_f32 v3, v4, v5
	s_nop 0
	v_cvt_pk_bf16_f32 v4, v6, v7
	v_cvt_pk_bf16_f32 v5, v8, v9
	global_store_dwordx4 v[30:31], v[2:5], off offset:256
	s_cbranch_vccnz .LBB0_2342
	s_andn2_b64 vcc, exec, s[2:3]
	s_cbranch_vccnz .LBB0_2341
	s_barrier
	s_branch .LBB0_2341
